# v90: v85 + M3 retention end-of-item barrier moved below the next item's address math and bulk load requests
# speedup vs baseline: 1.0015x; 1.0015x over previous
.LBB0_555:
	s_and_b32 s33, s3, 1
	s_lshl_b32 s4, s33, 1
	s_add_i32 s14, s4, s18
	s_mul_i32 s4, s10, 0x1100
	s_lshl_b32 s5, s11, 7
	s_add_i32 s45, s4, s5
	s_lshl_b32 s22, s14, 6
	v_or_b32_e32 v2, s45, v116
	v_mov_b64_e32 v[50:51], s[88:89]
	s_mul_i32 s5, s14, 0x44
	s_ashr_i32 s23, s22, 31
	v_mad_i64_i32 v[2:3], s[14:15], v2, s60, v[50:51]
	s_lshl_b64 s[14:15], s[22:23], 1
	v_mov_b32_e32 v101, v0
	v_lshl_add_u64 v[2:3], v[2:3], 0, s[14:15]
	v_or_b32_e32 v10, s45, v117
	v_lshl_add_u64 v[2:3], v[2:3], 0, v[100:101]
	v_mad_i64_i32 v[10:11], s[26:27], v10, s60, v[50:51]
	s_mul_i32 s4, s10, 0x110
	v_add_co_u32_e32 v6, vcc, s78, v2
	v_lshl_add_u64 v[10:11], v[10:11], 0, s[14:15]
	v_or_b32_e32 v18, s45, v118
	s_add_i32 s4, s4, s5
	v_addc_co_u32_e32 v7, vcc, 0, v3, vcc
	v_lshl_add_u64 v[10:11], v[10:11], 0, v[100:101]
	v_mad_i64_i32 v[18:19], s[26:27], v18, s60, v[50:51]
	s_add_i32 s4, s4, s11
	v_add_co_u32_e32 v14, vcc, s78, v10
	v_lshl_add_u64 v[18:19], v[18:19], 0, s[14:15]
	v_or_b32_e32 v26, s45, v119
	s_ashr_i32 s5, s4, 31
	v_addc_co_u32_e32 v15, vcc, 0, v11, vcc
	v_lshl_add_u64 v[18:19], v[18:19], 0, v[100:101]
	v_mad_i64_i32 v[26:27], s[26:27], v26, s60, v[50:51]
	s_lshl_b64 s[10:11], s[4:5], 13
	s_add_i32 s4, s4, 34
	v_add_co_u32_e32 v22, vcc, s78, v18
	v_lshl_add_u64 v[26:27], v[26:27], 0, s[14:15]
	s_ashr_i32 s5, s4, 31
	v_addc_co_u32_e32 v23, vcc, 0, v19, vcc
	v_lshl_add_u64 v[26:27], v[26:27], 0, v[100:101]
	s_lshl_b64 s[4:5], s[4:5], 13
	v_add_co_u32_e32 v30, vcc, s78, v26
	s_cmp_eq_u32 s33, 0
	s_nop 0
	v_addc_co_u32_e32 v31, vcc, 0, v27, vcc
	s_cselect_b64 vcc, -1, 0
	s_add_u32 s10, s66, s10
	s_addc_u32 s11, s67, s11
	s_add_u32 s4, s66, s4
	s_addc_u32 s5, s67, s5
	v_or_b32_e32 v104, s45, v109
	global_load_dwordx4 v[2:5], v[6:7], off offset:512
	s_nop 0
	global_load_dwordx4 v[6:9], v[6:7], off
	s_nop 0
	global_load_dwordx4 v[10:13], v[14:15], off offset:512
	s_nop 0
	global_load_dwordx4 v[14:17], v[14:15], off
	s_nop 0
	global_load_dwordx4 v[18:21], v[22:23], off offset:512
	s_nop 0
	global_load_dwordx4 v[22:25], v[22:23], off
	s_nop 0
	global_load_dwordx4 v[26:29], v[30:31], off offset:512
	s_nop 0
	global_load_dwordx4 v[30:33], v[30:31], off
	s_nop 0
	global_load_dwordx4 v[34:37], v125, s[10:11]
	global_load_dwordx4 v[38:41], v125, s[4:5]
	global_load_dwordx4 v[42:45], v126, s[10:11]
	global_load_dwordx4 v[46:49], v126, s[4:5]
	v_mad_i64_i32 v[106:107], s[4:5], v104, s60, v[50:51]
	v_lshl_add_u64 v[50:51], v[106:107], 0, s[14:15]
	v_mov_b32_e32 v103, v0
	v_lshl_add_u64 v[50:51], v[50:51], 0, v[102:103]
	global_load_dwordx4 v[78:81], v[50:51], off offset:3584
	global_load_dwordx4 v[74:77], v[50:51], off offset:3616
	global_load_dwordx4 v[70:73], v[50:51], off offset:3648
	global_load_dwordx4 v[66:69], v[50:51], off offset:3680
	v_cndmask_b32_e32 v50, v142, v1, vcc
	s_mov_b32 s10, 0
	v_mul_f32_e32 v101, 0xbfb8aa3b, v50
	v_ashrrev_i32_e32 v105, 31, v104
	s_mov_b64 s[4:5], -1
	s_barrier
	s_waitcnt vmcnt(15)
	ds_write_b128 v127, v[2:5]
	s_waitcnt vmcnt(14)
	ds_write_b128 v128, v[6:9] offset:16384
	s_waitcnt vmcnt(13)
	ds_write_b128 v129, v[10:13]
	s_waitcnt vmcnt(12)
	ds_write_b128 v130, v[14:17] offset:16384
	s_waitcnt vmcnt(11)
	ds_write_b128 v127, v[18:21] offset:8192
	s_waitcnt vmcnt(10)
	ds_write_b128 v131, v[22:25] offset:16384
	s_waitcnt vmcnt(9)
	ds_write_b128 v132, v[26:29] offset:8192
	s_waitcnt vmcnt(8)
	ds_write_b128 v133, v[30:33] offset:16384
	s_waitcnt vmcnt(7)
	ds_write_b128 v128, v[34:37] offset:32768
	s_waitcnt vmcnt(6)
	ds_write_b128 v128, v[38:41] offset:40960
	s_waitcnt vmcnt(5)
	ds_write_b128 v130, v[42:45] offset:32768
	s_waitcnt vmcnt(4)
	ds_write_b128 v130, v[46:49] offset:40960
	v_cndmask_b32_e32 v2, v143, v141, vcc
	v_mov_b32_e32 v18, 0
	v_mul_f32_e32 v103, 0xbfb8aa3b, v2
	v_mul_f32_e32 v167, 0xbf800000, v101
	v_mul_f32_e32 v168, 0xc0000000, v101
	v_mul_f32_e32 v169, 0xc0400000, v101
	v_mul_f32_e32 v170, 0xc1000000, v101
	v_mul_f32_e32 v171, 0x3f800000, v103
	v_mul_f32_e32 v172, 0x40000000, v103
	v_mul_f32_e32 v173, 0x40400000, v103
	v_mul_f32_e32 v174, 0x41000000, v103
	v_exp_f32_e32 v167, v167
	v_exp_f32_e32 v168, v168
	v_exp_f32_e32 v169, v169
	v_exp_f32_e32 v170, v170
	v_exp_f32_e32 v171, v171
	v_exp_f32_e32 v172, v172
	v_exp_f32_e32 v173, v173
	v_exp_f32_e32 v174, v174
	v_mov_b32_e32 v19, v18
	v_mov_b32_e32 v20, v18
	v_mov_b32_e32 v21, v18
	v_mov_b32_e32 v22, v18
	v_mov_b32_e32 v23, v18
	v_mov_b32_e32 v24, v18
	v_mov_b32_e32 v25, v18
	v_mov_b32_e32 v26, v18
	v_mov_b32_e32 v27, v18
	v_mov_b32_e32 v28, v18
	v_mov_b32_e32 v29, v18
	v_mov_b32_e32 v30, v18
	v_mov_b32_e32 v31, v18
	v_mov_b32_e32 v32, v18
	v_mov_b32_e32 v33, v18
	v_mov_b32_e32 v2, v18
	v_mov_b32_e32 v3, v18
	v_mov_b32_e32 v4, v18
	v_mov_b32_e32 v5, v18
	v_mov_b32_e32 v6, v18
	v_mov_b32_e32 v7, v18
	v_mov_b32_e32 v8, v18
	v_mov_b32_e32 v9, v18
	v_mov_b32_e32 v10, v18
	v_mov_b32_e32 v11, v18
	v_mov_b32_e32 v12, v18
	v_mov_b32_e32 v13, v18
	v_mov_b32_e32 v14, v18
	v_mov_b32_e32 v15, v18
	v_mov_b32_e32 v16, v18
	v_mov_b32_e32 v17, v18
	s_waitcnt lgkmcnt(0)
	s_barrier
	v_lshl_add_u64 v[152:153], s[22:23], 1, v[106:107]
	v_lshlrev_b32_e32 v154, 1, v82
	v_mov_b32_e32 v155, v0
	v_lshl_add_u64 v[152:153], v[152:153], 0, v[154:155]
	s_mov_b64 s[98:99], 0x1400
	ds_read_b64 v[156:157], v0 offset:640
	v_lshl_add_u64 v[154:155], v[152:153], 0, s[98:99]
	v_add_co_u32_e32 v152, vcc, s78, v152
	s_lshl_b64 s[98:99], s[24:25], 2
	s_lshl_b64 s[100:101], s[22:23], 2
	v_addc_co_u32_e32 v153, vcc, 0, v153, vcc
	global_load_dwordx2 v[222:223], v[152:153], off offset:1024
	global_load_dwordx2 v[224:225], v[154:155], off offset:16
	global_load_dwordx2 v[226:227], v[154:155], off offset:32
	global_load_dwordx2 v[228:229], v[154:155], off offset:48
	global_load_dwordx2 v[230:231], v[154:155], off offset:64
	global_load_dwordx2 v[232:233], v[154:155], off offset:80
	global_load_dwordx2 v[234:235], v[154:155], off offset:96
	global_load_dwordx2 v[236:237], v[154:155], off offset:112
	s_add_u32 s98, s98, s100
	s_addc_u32 s99, s99, s101
	s_waitcnt lgkmcnt(0)
	v_readfirstlane_b32 s100, v156
	v_readfirstlane_b32 s101, v157
	v_lshlrev_b32_e32 v152, 2, v82
	s_add_u32 s98, s100, s98
	s_addc_u32 s99, s101, s99
	global_load_dwordx4 v[238:241], v152, s[98:99]
	global_load_dwordx4 v[242:245], v152, s[98:99] offset:32
	global_load_dwordx4 v[246:249], v152, s[98:99] offset:64
	global_load_dwordx4 v[250:253], v152, s[98:99] offset:96
	global_load_dwordx4 v[200:203], v152, s[98:99] offset:128
	global_load_dwordx4 v[204:207], v152, s[98:99] offset:160
	global_load_dwordx4 v[214:217], v152, s[98:99] offset:192
	global_load_dwordx4 v[192:195], v152, s[98:99] offset:224
